# nt on the final-phase row loads / expert-output gathers and on the norm2 context rows' out-projection partial loads (read-once)
# speedup vs baseline: 1.0030x; 1.0010x over previous
.LBB0_1098:
	s_or_b64 exec, exec, s[12:13]
	s_and_saveexec_b64 s[12:13], s[0:1]
	s_cbranch_execz .LBB0_1100
	v_add_u32_e32 v98, 0xffffc000, v118
	v_mov_b32_e32 v99, v131
	v_lshlrev_b64 v[98:99], 11, v[98:99]
	v_lshl_add_u64 v[120:121], v[112:113], 0, v[98:99]
	v_add_co_u32_e32 v122, vcc, 0x400000, v120
	s_nop 1
	v_addc_co_u32_e32 v123, vcc, 0, v121, vcc
	v_add_co_u32_e32 v124, vcc, 0x800000, v120
	s_nop 1
	v_addc_co_u32_e32 v125, vcc, 0, v121, vcc
	v_add_co_u32_e32 v144, vcc, 0xc00000, v120
	s_nop 1
	v_addc_co_u32_e32 v145, vcc, 0, v121, vcc
	v_add_co_u32_e32 v146, vcc, 0x1000000, v120
	s_nop 1
	v_addc_co_u32_e32 v147, vcc, 0, v121, vcc
	v_add_co_u32_e32 v148, vcc, 0x1400000, v120
	s_nop 1
	v_addc_co_u32_e32 v149, vcc, 0, v121, vcc
	global_load_dwordx4 v[132:135], v[110:111], off
	global_load_dwordx4 v[136:139], v[110:111], off offset:1024
	global_load_dwordx4 v[140:143], v[110:111], off offset:2048
	global_load_dwordx4 v[98:101], v[110:111], off offset:3072
	global_load_dwordx2 v[150:151], v[120:121], off nt
	global_load_dwordx2 v[152:153], v[120:121], off offset:512 nt
	global_load_dwordx2 v[154:155], v[120:121], off offset:1024 nt
	global_load_dwordx2 v[156:157], v[120:121], off offset:1536 nt
	global_load_dwordx2 v[158:159], v[122:123], off nt
	global_load_dwordx2 v[160:161], v[122:123], off offset:512 nt
	global_load_dwordx2 v[162:163], v[122:123], off offset:1024 nt
	global_load_dwordx2 v[164:165], v[122:123], off offset:1536 nt
	global_load_dwordx2 v[166:167], v[124:125], off nt
	global_load_dwordx2 v[168:169], v[124:125], off offset:512 nt
	global_load_dwordx2 v[170:171], v[124:125], off offset:1024 nt
	global_load_dwordx2 v[126:127], v[124:125], off offset:1536 nt
	global_load_dwordx2 v[172:173], v[144:145], off nt
	global_load_dwordx2 v[174:175], v[144:145], off offset:512 nt
	global_load_dwordx2 v[176:177], v[144:145], off offset:1024 nt
	global_load_dwordx2 v[122:123], v[144:145], off offset:1536 nt
	s_nop 0
	global_load_dwordx2 v[144:145], v[146:147], off nt
	global_load_dwordx2 v[178:179], v[146:147], off offset:512 nt
	global_load_dwordx2 v[180:181], v[146:147], off offset:1024 nt
	global_load_dwordx2 v[124:125], v[146:147], off offset:1536 nt
	s_nop 0
	global_load_dwordx2 v[146:147], v[148:149], off nt
	global_load_dwordx2 v[182:183], v[148:149], off offset:512 nt
	global_load_dwordx2 v[184:185], v[148:149], off offset:1024 nt
	global_load_dwordx2 v[120:121], v[148:149], off offset:1536 nt
	s_waitcnt vmcnt(23)
	v_lshlrev_b32_e32 v186, 16, v150
	v_and_b32_e32 v187, 0xffff0000, v150
	v_lshlrev_b32_e32 v150, 16, v151
	v_and_b32_e32 v151, 0xffff0000, v151
	s_waitcnt vmcnt(19)
	v_lshlrev_b32_e32 v188, 16, v158
	v_and_b32_e32 v189, 0xffff0000, v158
	v_lshlrev_b32_e32 v158, 16, v159
	v_and_b32_e32 v159, 0xffff0000, v159
	v_pk_add_f32 v[186:187], v[186:187], v[188:189]
	v_pk_add_f32 v[150:151], v[150:151], v[158:159]
	s_waitcnt vmcnt(15)
	v_lshlrev_b32_e32 v158, 16, v166
	v_and_b32_e32 v159, 0xffff0000, v166
	v_lshlrev_b32_e32 v166, 16, v167
	v_and_b32_e32 v167, 0xffff0000, v167
	v_pk_add_f32 v[150:151], v[150:151], v[166:167]
	v_pk_add_f32 v[158:159], v[186:187], v[158:159]
	s_waitcnt vmcnt(11)
	v_lshlrev_b32_e32 v166, 16, v172
	v_and_b32_e32 v167, 0xffff0000, v172
	v_lshlrev_b32_e32 v172, 16, v173
	v_and_b32_e32 v173, 0xffff0000, v173
	s_waitcnt vmcnt(7)
	v_lshlrev_b32_e32 v186, 16, v144
	v_and_b32_e32 v187, 0xffff0000, v144
	v_lshlrev_b32_e32 v144, 16, v145
	v_and_b32_e32 v145, 0xffff0000, v145
	v_pk_add_f32 v[166:167], v[166:167], v[186:187]
	v_pk_add_f32 v[144:145], v[172:173], v[144:145]
	s_waitcnt vmcnt(3)
	v_lshlrev_b32_e32 v172, 16, v146
	v_and_b32_e32 v173, 0xffff0000, v146
	v_lshlrev_b32_e32 v146, 16, v147
	v_and_b32_e32 v147, 0xffff0000, v147
	v_mov_b32_e32 v148, v118
	v_mov_b32_e32 v149, v131
	v_pk_add_f32 v[144:145], v[144:145], v[146:147]
	v_pk_add_f32 v[146:147], v[166:167], v[172:173]
	v_lshlrev_b64 v[148:149], 12, v[148:149]
	v_pk_add_f32 v[146:147], v[158:159], v[146:147]
	v_pk_add_f32 v[144:145], v[150:151], v[144:145]
	v_pk_fma_f32 v[94:95], v[132:133], v[146:147], v[94:95]
	v_pk_fma_f32 v[96:97], v[134:135], v[144:145], v[96:97]
	v_lshl_add_u64 v[132:133], v[104:105], 0, v[148:149]
	global_store_dwordx4 v[132:133], v[94:97], off
	v_lshlrev_b32_e32 v132, 16, v152
	v_and_b32_e32 v133, 0xffff0000, v152
	v_lshlrev_b32_e32 v134, 16, v153
	v_and_b32_e32 v135, 0xffff0000, v153
	v_lshlrev_b32_e32 v144, 16, v160
	v_and_b32_e32 v145, 0xffff0000, v160
	v_lshlrev_b32_e32 v146, 16, v161
	v_and_b32_e32 v147, 0xffff0000, v161
	v_pk_add_f32 v[132:133], v[132:133], v[144:145]
	v_pk_add_f32 v[134:135], v[134:135], v[146:147]
	v_lshlrev_b32_e32 v144, 16, v168
	v_and_b32_e32 v145, 0xffff0000, v168
	v_lshlrev_b32_e32 v146, 16, v169
	v_and_b32_e32 v147, 0xffff0000, v169
	v_pk_add_f32 v[134:135], v[134:135], v[146:147]
	v_pk_add_f32 v[132:133], v[132:133], v[144:145]
	v_lshlrev_b32_e32 v144, 16, v174
	v_and_b32_e32 v145, 0xffff0000, v174
	v_lshlrev_b32_e32 v146, 16, v175
	v_and_b32_e32 v147, 0xffff0000, v175
	v_lshlrev_b32_e32 v150, 16, v178
	v_and_b32_e32 v151, 0xffff0000, v178
	v_lshlrev_b32_e32 v152, 16, v179
	v_and_b32_e32 v153, 0xffff0000, v179
	v_pk_add_f32 v[144:145], v[144:145], v[150:151]
	v_pk_add_f32 v[146:147], v[146:147], v[152:153]
	s_waitcnt vmcnt(3)
	v_lshlrev_b32_e32 v150, 16, v182
	v_and_b32_e32 v151, 0xffff0000, v182
	v_lshlrev_b32_e32 v152, 16, v183
	v_and_b32_e32 v153, 0xffff0000, v183
	v_pk_add_f32 v[146:147], v[146:147], v[152:153]
	v_pk_add_f32 v[144:145], v[144:145], v[150:151]
	v_pk_add_f32 v[134:135], v[134:135], v[146:147]
	v_pk_add_f32 v[132:133], v[132:133], v[144:145]
	v_pk_fma_f32 v[92:93], v[138:139], v[134:135], v[92:93]
	v_pk_fma_f32 v[90:91], v[136:137], v[132:133], v[90:91]
	v_lshlrev_b32_e32 v136, 16, v154
	v_and_b32_e32 v137, 0xffff0000, v154
	v_lshlrev_b32_e32 v138, 16, v155
	v_and_b32_e32 v139, 0xffff0000, v155
	v_lshlrev_b32_e32 v144, 16, v162
	v_and_b32_e32 v145, 0xffff0000, v162
	v_lshlrev_b32_e32 v146, 16, v163
	v_and_b32_e32 v147, 0xffff0000, v163
	v_pk_add_f32 v[136:137], v[136:137], v[144:145]
	v_pk_add_f32 v[138:139], v[138:139], v[146:147]
	v_lshlrev_b32_e32 v144, 16, v170
	v_and_b32_e32 v145, 0xffff0000, v170
	v_lshlrev_b32_e32 v146, 16, v171
	v_and_b32_e32 v147, 0xffff0000, v171
	v_lshl_add_u64 v[132:133], v[106:107], 0, v[148:149]
	v_pk_add_f32 v[138:139], v[138:139], v[146:147]
	v_pk_add_f32 v[136:137], v[136:137], v[144:145]
	v_lshlrev_b32_e32 v144, 16, v176
	v_and_b32_e32 v145, 0xffff0000, v176
	v_lshlrev_b32_e32 v146, 16, v177
	v_and_b32_e32 v147, 0xffff0000, v177
	v_lshlrev_b32_e32 v148, 16, v180
	v_and_b32_e32 v149, 0xffff0000, v180
	v_lshlrev_b32_e32 v150, 16, v181
	v_and_b32_e32 v151, 0xffff0000, v181
	v_pk_add_f32 v[144:145], v[144:145], v[148:149]
	v_pk_add_f32 v[146:147], v[146:147], v[150:151]
	s_waitcnt vmcnt(2)
	v_lshlrev_b32_e32 v148, 16, v184
	v_and_b32_e32 v149, 0xffff0000, v184
	v_lshlrev_b32_e32 v150, 16, v185
	v_and_b32_e32 v151, 0xffff0000, v185
	s_movk_i32 s0, 0x3000
	v_pk_add_f32 v[146:147], v[146:147], v[150:151]
	v_pk_add_f32 v[144:145], v[144:145], v[148:149]
	v_add_co_u32_e32 v134, vcc, s0, v132
	v_pk_add_f32 v[136:137], v[136:137], v[144:145]
	v_pk_add_f32 v[138:139], v[138:139], v[146:147]
	v_addc_co_u32_e32 v135, vcc, 0, v133, vcc
	v_pk_fma_f32 v[88:89], v[142:143], v[138:139], v[88:89]
	v_pk_fma_f32 v[86:87], v[140:141], v[136:137], v[86:87]
	global_store_dwordx4 v[134:135], v[90:93], off offset:2560
	global_store_dwordx4 v[134:135], v[86:89], off offset:3584
	v_lshlrev_b32_e32 v134, 16, v156
	v_and_b32_e32 v135, 0xffff0000, v156
	v_lshlrev_b32_e32 v136, 16, v157
	v_and_b32_e32 v137, 0xffff0000, v157
	v_lshlrev_b32_e32 v138, 16, v164
	v_and_b32_e32 v139, 0xffff0000, v164
	v_lshlrev_b32_e32 v140, 16, v165
	v_and_b32_e32 v141, 0xffff0000, v165
	v_pk_add_f32 v[134:135], v[134:135], v[138:139]
	v_pk_add_f32 v[136:137], v[136:137], v[140:141]
	v_lshlrev_b32_e32 v138, 16, v126
	v_and_b32_e32 v139, 0xffff0000, v126
	v_lshlrev_b32_e32 v126, 16, v127
	v_and_b32_e32 v127, 0xffff0000, v127
	v_pk_add_f32 v[126:127], v[136:137], v[126:127]
	v_pk_add_f32 v[134:135], v[134:135], v[138:139]
	v_lshlrev_b32_e32 v136, 16, v122
	v_and_b32_e32 v137, 0xffff0000, v122
	v_lshlrev_b32_e32 v122, 16, v123
	v_and_b32_e32 v123, 0xffff0000, v123
	v_lshlrev_b32_e32 v138, 16, v124
	v_and_b32_e32 v139, 0xffff0000, v124
	v_lshlrev_b32_e32 v124, 16, v125
	v_and_b32_e32 v125, 0xffff0000, v125
	v_pk_add_f32 v[136:137], v[136:137], v[138:139]
	v_pk_add_f32 v[122:123], v[122:123], v[124:125]
	s_waitcnt vmcnt(3)
	v_lshlrev_b32_e32 v124, 16, v120
	v_and_b32_e32 v125, 0xffff0000, v120
	v_lshlrev_b32_e32 v120, 16, v121
	v_and_b32_e32 v121, 0xffff0000, v121
	v_pk_add_f32 v[120:121], v[122:123], v[120:121]
	v_pk_add_f32 v[122:123], v[136:137], v[124:125]
	v_pk_add_f32 v[120:121], v[126:127], v[120:121]
	v_pk_add_f32 v[122:123], v[134:135], v[122:123]
	v_pk_fma_f32 v[84:85], v[100:101], v[120:121], v[84:85]
	v_pk_fma_f32 v[82:83], v[98:99], v[122:123], v[82:83]
	v_add_co_u32_e32 v98, vcc, 0x4000, v132
	s_nop 1
	v_addc_co_u32_e32 v99, vcc, 0, v133, vcc
	global_store_dwordx4 v[98:99], v[82:85], off offset:512

.LBB0_1480:
	v_readlane_b32 s0, v253, 22
	v_and_b32_e32 v64, 63, v0
	v_ashrrev_i32_e32 v0, 3, v0
	v_and_b32_e32 v0, -8, v0
	v_add_u32_e32 v66, s0, v0
	v_ashrrev_i32_e32 v67, 31, v66
	v_readlane_b32 s0, v251, 51
	v_lshlrev_b64 v[0:1], 12, v[66:67]
	v_readlane_b32 s1, v251, 52
	v_mov_b32_e32 v77, 0
	v_lshlrev_b32_e32 v76, 4, v64
	v_lshl_add_u64 v[0:1], s[0:1], 0, v[0:1]
	v_lshl_add_u64 v[0:1], v[0:1], 0, v[76:77]
	global_load_dwordx4 v[28:31], v[0:1], off nt
	global_load_dwordx4 v[24:27], v[0:1], off offset:1024 nt
	global_load_dwordx4 v[20:23], v[0:1], off offset:2048 nt
	global_load_dwordx4 v[16:19], v[0:1], off offset:3072 nt
	v_or_b32_e32 v0, 1, v66
	v_ashrrev_i32_e32 v1, 31, v0
	v_lshlrev_b64 v[0:1], 12, v[0:1]
	v_lshl_add_u64 v[0:1], s[0:1], 0, v[0:1]
	v_lshl_add_u64 v[32:33], v[0:1], 0, v[76:77]
	global_load_dwordx4 v[0:3], v[32:33], off nt
	global_load_dwordx4 v[4:7], v[32:33], off offset:1024 nt
	global_load_dwordx4 v[8:11], v[32:33], off offset:2048 nt
	global_load_dwordx4 v[12:15], v[32:33], off offset:3072 nt
	v_lshlrev_b32_e32 v32, 2, v64
	v_cmp_gt_u32_e64 s[0:1], 16, v64
	v_cmp_lt_u32_e32 vcc, 15, v64
	v_mov_b32_e32 v65, v77
	s_and_saveexec_b64 s[2:3], vcc
	s_xor_b64 s[2:3], exec, s[2:3]
	v_mov_b32_e32 v65, 0
	s_or_saveexec_b64 s[2:3], s[2:3]
	v_mov_b32_e32 v101, 2.0
	s_xor_b64 exec, exec, s[2:3]
	s_cbranch_execz .LBB0_1484
	v_lshlrev_b64 v[34:35], 6, v[66:67]
	v_lshl_or_b32 v34, v64, 2, v34
	v_lshl_add_u64 v[36:37], s[86:87], 0, v[34:35]
	v_lshl_add_u64 v[34:35], s[96:97], 0, v[34:35]
	global_load_dword v101, v[36:37], off
	global_load_dword v77, v[34:35], off

.LBB0_1486:
	s_waitcnt vmcnt(0)
	v_mov_b64_e32 v[58:59], v[2:3]
	v_mov_b64_e32 v[54:55], v[6:7]
	v_mov_b64_e32 v[50:51], v[10:11]
	v_mov_b64_e32 v[62:63], v[14:15]
	v_mov_b64_e32 v[56:57], v[0:1]
	v_mov_b64_e32 v[52:53], v[4:5]
	v_mov_b64_e32 v[48:49], v[8:9]
	s_cmp_gt_u32 s8, 5
	v_mov_b64_e32 v[60:61], v[12:13]
	s_cbranch_scc1 .LBB0_1488
	v_add_u32_e32 v0, s8, v76
	v_ashrrev_i32_e32 v1, 31, v0
	v_lshlrev_b64 v[0:1], 12, v[0:1]
	v_lshl_add_u64 v[78:79], v[70:71], 0, v[0:1]
	global_load_dwordx4 v[0:3], v[78:79], off nt
	global_load_dwordx4 v[4:7], v[78:79], off offset:1024 nt
	global_load_dwordx4 v[8:11], v[78:79], off offset:2048 nt
	global_load_dwordx4 v[12:15], v[78:79], off offset:3072 nt

.LBB0_1494:
	s_add_u32 s14, s8, -1
	s_addc_u32 s15, s9, -1
	s_and_b64 vcc, s[14:15], s[8:9]
	s_mulk_i32 s12, 0x900
	s_ashr_i32 s9, s13, 31
	s_add_u32 s8, s13, s12
	s_addc_u32 s9, s9, 0
	v_lshl_add_u64 v[104:105], s[8:9], 0, v[96:97]
	s_mulk_i32 s7, 0x900
	s_ashr_i32 s9, s3, 31
	s_add_u32 s8, s7, s3
	s_addc_u32 s9, 0, s9
	v_lshl_add_u64 v[112:113], s[8:9], 0, v[96:97]
	v_lshlrev_b64 v[104:105], 11, v[104:105]
	v_lshlrev_b64 v[112:113], 11, v[112:113]
	v_lshl_add_u64 v[104:105], v[74:75], 0, v[104:105]
	v_lshl_add_u64 v[112:113], v[74:75], 0, v[112:113]
	global_load_dwordx2 v[106:107], v[104:105], off nt
	global_load_dwordx2 v[108:109], v[104:105], off offset:512 nt
	global_load_dwordx2 v[110:111], v[104:105], off offset:1024 nt
	s_cmp_eq_u64 vcc, 0
	global_load_dwordx2 v[104:105], v[104:105], off offset:1536 nt
	s_nop 0
	global_load_dwordx2 v[114:115], v[112:113], off nt
	global_load_dwordx2 v[116:117], v[112:113], off offset:512 nt
	global_load_dwordx2 v[118:119], v[112:113], off offset:1024 nt
	global_load_dwordx2 v[120:121], v[112:113], off offset:1536 nt
	s_waitcnt vmcnt(7)
	v_lshlrev_b32_e32 v112, 16, v106
	v_and_b32_e32 v113, 0xffff0000, v106
	s_waitcnt vmcnt(3)
	v_lshlrev_b32_e32 v128, 16, v114
	v_and_b32_e32 v129, 0xffff0000, v114
	v_lshlrev_b32_e32 v114, 16, v115
	v_and_b32_e32 v115, 0xffff0000, v115
	s_waitcnt vmcnt(2)
	v_lshlrev_b32_e32 v130, 16, v116
	v_and_b32_e32 v131, 0xffff0000, v116
	v_lshlrev_b32_e32 v116, 16, v117
	v_and_b32_e32 v117, 0xffff0000, v117
	s_waitcnt vmcnt(1)
	v_lshlrev_b32_e32 v132, 16, v118
	v_and_b32_e32 v133, 0xffff0000, v118
	v_lshlrev_b32_e32 v118, 16, v119
	v_and_b32_e32 v119, 0xffff0000, v119
	s_waitcnt vmcnt(0)
	v_lshlrev_b32_e32 v134, 16, v120
	v_and_b32_e32 v135, 0xffff0000, v120
	v_lshlrev_b32_e32 v120, 16, v121
	v_and_b32_e32 v121, 0xffff0000, v121
	v_lshlrev_b32_e32 v106, 16, v107
	v_and_b32_e32 v107, 0xffff0000, v107
	v_lshlrev_b32_e32 v122, 16, v108
	v_and_b32_e32 v123, 0xffff0000, v108
	v_lshlrev_b32_e32 v108, 16, v109
	v_and_b32_e32 v109, 0xffff0000, v109
	v_lshlrev_b32_e32 v124, 16, v110
	v_and_b32_e32 v125, 0xffff0000, v110
	v_lshlrev_b32_e32 v110, 16, v111
	v_and_b32_e32 v111, 0xffff0000, v111
	v_lshlrev_b32_e32 v126, 16, v104
	v_and_b32_e32 v127, 0xffff0000, v104
	v_lshlrev_b32_e32 v104, 16, v105
	v_and_b32_e32 v105, 0xffff0000, v105
	v_pk_mul_f32 v[120:121], s[6:7], v[120:121] op_sel_hi:[0,1]
	v_pk_mul_f32 v[134:135], s[6:7], v[134:135] op_sel_hi:[0,1]
	v_pk_mul_f32 v[118:119], s[6:7], v[118:119] op_sel_hi:[0,1]
	v_pk_mul_f32 v[132:133], s[6:7], v[132:133] op_sel_hi:[0,1]
	v_pk_mul_f32 v[116:117], s[6:7], v[116:117] op_sel_hi:[0,1]
	v_pk_mul_f32 v[130:131], s[6:7], v[130:131] op_sel_hi:[0,1]
	v_pk_mul_f32 v[114:115], s[6:7], v[114:115] op_sel_hi:[0,1]
	v_pk_mul_f32 v[128:129], s[6:7], v[128:129] op_sel_hi:[0,1]
	v_pk_fma_f32 v[112:113], s[2:3], v[112:113], v[128:129] op_sel_hi:[0,1,1]
	v_pk_fma_f32 v[106:107], s[2:3], v[106:107], v[114:115] op_sel_hi:[0,1,1]
	v_pk_fma_f32 v[114:115], s[2:3], v[122:123], v[130:131] op_sel_hi:[0,1,1]
	v_pk_fma_f32 v[108:109], s[2:3], v[108:109], v[116:117] op_sel_hi:[0,1,1]
	v_pk_fma_f32 v[116:117], s[2:3], v[124:125], v[132:133] op_sel_hi:[0,1,1]
	v_pk_fma_f32 v[110:111], s[2:3], v[110:111], v[118:119] op_sel_hi:[0,1,1]
	v_pk_fma_f32 v[118:119], s[2:3], v[126:127], v[134:135] op_sel_hi:[0,1,1]
	v_pk_fma_f32 v[104:105], s[2:3], v[104:105], v[120:121] op_sel_hi:[0,1,1]
	v_pk_add_f32 v[86:87], v[86:87], v[104:105]
	v_pk_add_f32 v[80:81], v[80:81], v[118:119]
	v_pk_add_f32 v[88:89], v[88:89], v[110:111]
	v_pk_add_f32 v[82:83], v[82:83], v[116:117]
	v_pk_add_f32 v[92:93], v[92:93], v[108:109]
	v_pk_add_f32 v[84:85], v[84:85], v[114:115]
	v_pk_add_f32 v[94:95], v[94:95], v[106:107]
	v_pk_add_f32 v[90:91], v[90:91], v[112:113]
	s_cbranch_scc1 .LBB0_1485
